# MoE gate/up fp6 conversion of experts 0-3 moved out of P0 into the dense FFN gate/up GEMM unit epilogues (two 32-load items per unit per wave, loads issued at epilogue start / midpoint)
# speedup vs baseline: 1.0096x; 1.0096x over previous
; template <int MODE>
; __device__ __forceinline__ void tr_matrix6(const float* W, int nb, int K, int N, unsigned char* WT, int drows, int rot, int gw, int NGW, int lane, float wscale) {
;     const int nbn = N / 32, per = (K / 256) * nbn, total = nb * per;
;     int it = gw - rot; if (it < 0) it += NGW;
;     const int c = lane & 7, q = lane >> 3;
;     for (; it < total; it += NGW) {
; __global__ void __launch_bounds__(NTHREADS, 2) fwd_kernel(Args args) {
;     ...
;         tr_matrix6<1>(args.in[I_MOEG], NE, D, FF, ws + W_MOEGU, 2 * FF, R9, gw, NGW, lane, WSC6);
.LBB0_54:
	s_add_u32 s40, s70, 0x8a00000
	s_addc_u32 s41, s71, 0
	v_readlane_b32 s6, v251, 9
	s_cmpk_lt_i32 s6, 0x7d0
	s_cselect_b32 s0, s72, 0
	s_add_i32 s0, s6, s0
	s_add_i32 s3, s0, 0xfffff830
	s_cmpk_gt_i32 s3, 0x37ff
	v_readlane_b32 s7, v251, 10
	s_branch .LBB0_59
	v_readlane_b32 s48, v251, 29
	v_readlane_b32 s60, v251, 41
	v_readlane_b32 s61, v251, 42
	v_and_b32_e32 v132, 28, v144
	v_mov_b32_e32 v130, 0
	v_readlane_b32 s62, v251, 43
	v_readlane_b32 s63, v251, 44
	s_mov_b64 s[20:21], s[60:61]
	v_and_b32_e32 v146, 0xe0, v144
	v_mov_b32_e32 v147, v130
	s_movk_i32 s0, 0x7000
	v_lshlrev_b32_e32 v148, 2, v132
	v_mov_b32_e32 v149, v130
	s_mov_b32 s1, 0x93000
	s_mov_b32 s5, 0x9a000
	s_mov_b32 s14, 0xa1000
	s_mov_b32 s15, 0xa8000
	s_mov_b32 s16, 0xaf000
	s_mov_b32 s17, 0xb6000
	s_mov_b32 s33, 0xbd000
	s_mov_b32 s38, 0xc4000
	s_mov_b32 s39, 0xcb000
	s_mov_b32 s42, 0xd2000
	s_mov_b32 s43, 0xd9000
	s_mov_b32 s44, 0xc0f00000
	v_mov_b32_e32 v133, 0x40f00000
	s_movk_i32 s45, 0x1000
	s_mov_b32 s46, s3
	s_mov_b64 s[22:23], s[62:63]
	v_readlane_b32 s49, v251, 30
	v_readlane_b32 s50, v251, 31
	v_readlane_b32 s51, v251, 32
	v_readlane_b32 s52, v251, 33
	v_readlane_b32 s53, v251, 34
	v_readlane_b32 s54, v251, 35
	v_readlane_b32 s55, v251, 36
	v_readlane_b32 s56, v251, 37
	v_readlane_b32 s57, v251, 38
	v_readlane_b32 s58, v251, 39
	v_readlane_b32 s59, v251, 40

;     ...
;     const int tid = opaque_tid(), wid = __builtin_amdgcn_readfirstlane(tid >> 6), lane = tid & 63, wr = wid >> 2, wc = wid & 3, fr = lane & 15, fq = lane >> 4;
;     const int K = g.K, nt = K / 128;
;     unsigned voffA[2], voffB[2];
; #pragma unroll
;     for (int i = 0; i < 2; ++i) { int R, C; stage_rc8(tid * 16 + i * 8192, R, C); const int Rb = Epi::PERM ? ((R & ~31) + perm32(R & 31)) : R;
;         voffA[i] = (unsigned)(R * g.lda + C); voffB[i] = (unsigned)(Rb * g.ldb + C); }
;     const size_t kstep = 128;
;     const size_t hstepA = (size_t)HALF * g.lda, hstepB = (size_t)HALF * g.ldb;
;     const unsigned ldsw = (unsigned)wid * 1024u;
;     const int aoff0 = lds_byte8(wr * 64 + fr, 2 * fq), aoff1 = lds_byte8(wr * 64 + fr, 2 * fq + 1), boff0 = lds_byte8(wc * 32 + fr, 2 * fq), boff1 = lds_byte8(wc * 32 + fr, 2 * fq + 1);
;     ...
;     Unit cur, nxt; int ui = 0;
;     if (!S.next(0, cur)) return;
;     Acc acc;
; #pragma unroll
;     for (int a = 0; a < 2; ++a)
; #pragma unroll
;         for (int b = 0; b < 2; ++b)
; #pragma unroll
;             for (int m = 0; m < 4; ++m)
; #pragma unroll
;                 for (int n = 0; n < 2; ++n) acc[a][b][m][n] = (f32x4){0.f, 0.f, 0.f, 0.f};
;     typename Frag8<FP6>::T At[4], B0[2], B1[2];
;     const char* cA = (const char*)g.A + cur.aoff; const char* cB = (const char*)g.Bt + cur.boff;
;     S.a_ready(cur);
;     PG8_STAGE(PG8_SB(0, 0), cB, voffB); PG8_STAGE(PG8_SB(0, 1), cB + hstepB, voffB); PG8_STAGE(PG8_SA(0, 0), cA, voffA); PG8_STAGE(PG8_SA(0, 1), cA + hstepA, voffA);
;     if (wr == 1) PG8_BAR;
;     PG8_WAIT_V(2); PG8_BAR;
;     PG8_STAGE(PG8_SB(1, 0), cB + kstep, voffB); PG8_STAGE(PG8_SA(1, 0), cA + kstep, voffA); PG8_STAGE(PG8_SB(1, 1), cB + hstepB + kstep, voffB);
;     PG8_WAIT_V(6); PG8_BAR;
; template <int MODE>
; __device__ __forceinline__ void tr_matrix6(const float* W, int nb, int K, int N, unsigned char* WT, int drows, int rot, int gw, int NGW, int lane, float wscale) {
;     ...
;         const float* src = W + (size_t)e * K * N + (size_t)(k0 + 32 * q) * N + n0 + 4 * c;
;         f32x4 v[32];
; #pragma unroll
;         for (int i = 0; i < 32; ++i) v[i] = *(const f32x4*)(src + (size_t)i * N);
;         const int drow0 = (MODE == 0) ? n0 : ((n0 >> 7) * 256 + (n0 & 127) + (MODE == 2 ? 128 : 0));
;         unsigned char* dst = WT + (size_t)e * drows * K + (size_t)(drow0 + 4 * c) * K + k0 + 32 * q;
.LBB0_585:
	s_or_b64 exec, exec, s[4:5]
	v_mov_b32_e32 v12, v0
	s_waitcnt lgkmcnt(0)
	s_barrier
	v_readlane_b32 s98, v251, 9
	v_readlane_b32 s100, v251, 0
	v_readlane_b32 s101, v251, 1
	v_mbcnt_lo_u32_b32 v248, -1, 0
	v_mbcnt_hi_u32_b32 v248, -1, v248
	s_nop 3
	s_sub_u32 s100, s100, 0x38
	s_subb_u32 s101, s101, 0
	s_lshr_b32 s4, s98, 10
	s_lshl_b32 s5, s4, 3
	s_add_u32 s100, s100, s5
	s_addc_u32 s101, s101, 0
	s_load_dwordx2 s[100:101], s[100:101], 0x0
	s_lshr_b32 s6, s98, 2
	s_and_b32 s6, s6, 63
	s_lshr_b32 s8, s98, 8
	s_and_b32 s8, s8, 3
	s_and_b32 s10, s98, 3
	s_mul_i32 s10, s10, 28
	s_lshl_b32 s5, s8, 11
	s_lshl_b32 s99, s6, 5
	s_add_u32 s5, s5, s99
	s_mul_i32 s5, s5, 0x7000
	s_lshl_b32 s99, s10, 8
	s_add_u32 s5, s5, s99
	s_waitcnt lgkmcnt(0)
	s_add_u32 s100, s100, s5
	s_addc_u32 s101, s101, 0
	v_writelane_b32 v252, s100, 4
	v_writelane_b32 v252, s101, 5
	s_lshl_b32 s4, s4, 7
	s_mul_i32 s5, s8, 0x3800
	s_add_u32 s4, s4, s5
	s_lshr_b32 s5, s10, 1
	s_lshl_b32 s5, s5, 8
	s_add_u32 s4, s4, s5
	s_lshl_b32 s4, s4, 11
	s_lshl_b32 s5, s6, 5
	s_add_u32 s4, s4, s5
	s_add_u32 s4, s4, 0x8a00000
	s_add_u32 s100, s70, s4
	s_addc_u32 s101, s71, 0
	v_writelane_b32 v252, s100, 6
	v_writelane_b32 v252, s101, 7
	v_lshlrev_b32_e32 v249, 11, v248
	v_lshlrev_b32_e32 v248, 2, v248
	v_mov_b32_e32 v254, 0x40f00000
	v_mov_b32_e32 v255, 0xc0f00000
	v_mov_b32_e32 v246, 0
	v_mov_b32_e32 v247, 0
	s_mov_b32 s98, 0
	s_cmpk_lt_i32 s2, 0xe00
	s_nop 0
	v_readfirstlane_b32 s1, v12
	s_cbranch_scc0 .LBB0_601
	v_lshlrev_b32_e32 v2, 4, v12
	v_add_u32_e32 v3, 0x2000, v2
	v_ashrrev_i32_e32 v10, 7, v3
	v_bfe_u32 v5, v3, 7, 2
	s_mov_b32 s4, 0x1fffe0
	v_and_or_b32 v5, v10, s4, v5
	v_bfe_u32 v11, v3, 7, 4
	s_mov_b32 s4, 0x1ffff0
	v_ashrrev_i32_e32 v13, 3, v12
	v_bfe_u32 v14, v2, 7, 4
	v_and_or_b32 v7, v10, s4, v11
	v_and_or_b32 v8, v13, s4, v14
	s_lshr_b32 s4, s3, 29
	s_add_i32 s4, s2, s4
	s_ashr_i32 s8, s1, 6
	s_ashr_i32 s6, s4, 3
	s_and_b32 s4, s4, -8
	s_ashr_i32 s5, s1, 8
	s_lshl_b32 s0, s8, 10
	s_sub_i32 s4, s2, s4
	s_cmp_lt_i32 s4, 0
	s_movk_i32 s10, 0x1c1
	s_cselect_b32 s7, s10, 0x1c0
	s_mul_i32 s4, s4, s7
	s_add_i32 s4, s4, s6
	s_mul_hi_i32 s6, s4, 0x92492493
	s_add_i32 s6, s6, s4
	s_lshr_b32 s7, s6, 31
	s_ashr_i32 s6, s6, 8
	s_add_i32 s6, s6, s7
	s_lshl_b32 s7, s6, 3
	s_mulk_i32 s6, 0x1c0
	s_sub_i32 s6, s4, s6
	s_sext_i32_i16 s4, s6
	v_lshrrev_b32_e32 v4, 7, v3
	v_lshrrev_b32_e32 v6, 2, v10
	v_lshrrev_b32_e32 v3, 6, v3
	s_bfe_u32 s4, s4, 0x3001c
	v_and_b32_e32 v6, 4, v6
	v_and_b32_e32 v3, 24, v3
	s_add_i32 s9, s6, s4
	v_or3_b32 v3, v5, v6, v3
	v_bfe_u32 v5, v4, 3, 1
	s_sext_i32_i16 s4, s9
	s_and_b32 s9, s9, 0xfff8
	v_and_or_b32 v4, v4, 6, v5
	s_sub_i32 s6, s6, s9
	v_lshlrev_b32_e32 v3, 11, v3
	v_lshlrev_b32_e32 v4, 4, v4
	v_and_b32_e32 v5, 0x70, v2
	s_sext_i32_i16 s6, s6
	v_bitop3_b32 v162, v3, v4, v5 bitop3:0xf6
	v_lshlrev_b32_e32 v3, 11, v7
	s_lshr_b32 s4, s4, 3
	s_add_i32 s56, s7, s6
	v_bitop3_b32 v164, v4, v3, v5 bitop3:0xde
	v_bfe_u32 v3, v12, 3, 25
	v_and_b32_e32 v6, 0x1fffe0, v13
	v_lshrrev_b32_e32 v7, 2, v13
	v_lshrrev_b32_e32 v9, 2, v12
	s_bfe_i64 s[6:7], s[4:5], 0x100000
	s_ashr_i32 s57, s56, 31
	v_and_or_b32 v6, v3, 3, v6
	v_and_b32_e32 v7, 4, v7
	v_and_b32_e32 v9, 24, v9
	s_lshl_b64 s[6:7], s[6:7], 19
	s_lshl_b64 s[12:13], s[56:57], 19
	v_readlane_b32 s9, v251, 51
	v_or3_b32 v6, v6, v7, v9
	v_bfe_u32 v7, v3, 3, 1
	s_add_u32 s58, s9, s6
	v_readlane_b32 s6, v251, 52
	v_and_or_b32 v3, v3, 6, v7
	s_addc_u32 s59, s6, s7
	s_add_i32 s11, s0, 0
	v_lshlrev_b32_e32 v6, 11, v6
	v_lshlrev_b32_e32 v3, 4, v3
	s_add_i32 s24, s11, 0x10000
	s_add_i32 s25, s11, 0x12000
	v_bitop3_b32 v166, v6, v3, v5 bitop3:0xf6
	s_mov_b32 m0, s24
	s_add_u32 s6, s58, 0x40000
	global_load_lds_dwordx4 v166, s[58:59]
	s_mov_b32 m0, s25
	s_addc_u32 s7, s59, 0
	s_add_i32 s66, s11, 0x14000
	s_add_i32 s67, s11, 0x16000
	global_load_lds_dwordx4 v162, s[58:59]
	s_mov_b32 m0, s66
	s_add_u32 s60, s14, s12
	v_lshlrev_b32_e32 v6, 11, v8
	global_load_lds_dwordx4 v166, s[6:7]
	s_mov_b32 m0, s67
	s_addc_u32 s61, s15, s13
	s_add_i32 s0, s11, 0x2000
	v_bitop3_b32 v168, v3, v6, v5 bitop3:0xde
	global_load_lds_dwordx4 v162, s[6:7]
	s_mov_b32 m0, s11
	s_add_u32 s6, s60, 0x40000
	global_load_lds_dwordx4 v168, s[60:61]
	s_mov_b32 m0, s0
	s_addc_u32 s7, s61, 0
	s_add_i32 s78, s11, 0x4000
	global_load_lds_dwordx4 v164, s[60:61]
	s_mov_b32 m0, s78
	s_add_i32 s79, s11, 0x6000
	global_load_lds_dwordx4 v168, s[6:7]
	s_mov_b32 m0, s79
	v_mov_b32_e32 v167, 0
	global_load_lds_dwordx4 v164, s[6:7]
	s_movk_i32 s6, 0x70
	v_mov_b32_e32 v163, v167
	v_mov_b32_e32 v169, v167
	v_mov_b32_e32 v165, v167
	s_cmp_eq_u32 s5, 1
	v_bitop3_b32 v15, v4, v2, s6 bitop3:0x78
	v_bitop3_b32 v16, v3, v2, s6 bitop3:0x78
	s_mov_b32 s80, 0
	v_lshl_add_u64 v[8:9], s[58:59], 0, v[166:167]
	v_lshl_add_u64 v[6:7], s[58:59], 0, v[162:163]
	v_lshl_add_u64 v[2:3], s[60:61], 0, v[168:169]
	s_cselect_b64 s[6:7], -1, 0
	s_cmp_lg_u32 s5, 1
	v_lshl_add_u64 v[4:5], s[60:61], 0, v[164:165]
	s_cbranch_scc1 .LBB0_588
	s_barrier

;     ...
;         if constexpr (MODE == 2) {
; #pragma unroll
;             for (int a = 0; a < 2; ++a)
; #pragma unroll
;                 for (int b = 0; b < 2; ++b)
; #pragma unroll
;                     for (int m = 0; m < 4; ++m)
; #pragma unroll
;                         for (int n = 0; n < 2; ++n)
;                         { const f32x4 t_ = acc[a][b][m][n]; f32x4 r_;
;                           r_.x = (float)__float_as_int(t_.x); r_.y = (float)__float_as_int(t_.y); r_.z = (float)__float_as_int(t_.z); r_.w = (float)__float_as_int(t_.w); acc[a][b][m][n] = r_; }
;         }
; template <int MODE>
; __device__ __forceinline__ void tr_matrix6(const float* W, int nb, int K, int N, unsigned char* WT, int drows, int rot, int gw, int NGW, int lane, float wscale) {
;     ...
;         const float* src = W + (size_t)e * K * N + (size_t)(k0 + 32 * q) * N + n0 + 4 * c;
;         f32x4 v[32];
; #pragma unroll
;         for (int i = 0; i < 32; ++i) v[i] = *(const f32x4*)(src + (size_t)i * N);
.LBB0_597:
	s_cmp_lt_u32 s98, 28
	s_cbranch_scc0 .Lp8f_s
	v_readlane_b32 s100, v252, 4
	v_readlane_b32 s101, v252, 5
	s_lshl_b32 s99, s98, 8
	s_nop 1
	s_add_u32 s100, s100, s99
	s_addc_u32 s101, s101, 0
	global_load_dword v208, v248, s[100:101]
	s_add_u32 s100, s100, 0x7000
	s_addc_u32 s101, s101, 0
	global_load_dword v209, v248, s[100:101]
	s_add_u32 s100, s100, 0x7000
	s_addc_u32 s101, s101, 0
	global_load_dword v210, v248, s[100:101]
	s_add_u32 s100, s100, 0x7000
	s_addc_u32 s101, s101, 0
	global_load_dword v211, v248, s[100:101]
	s_add_u32 s100, s100, 0x7000
	s_addc_u32 s101, s101, 0
	global_load_dword v212, v248, s[100:101]
	s_add_u32 s100, s100, 0x7000
	s_addc_u32 s101, s101, 0
	global_load_dword v213, v248, s[100:101]
	s_add_u32 s100, s100, 0x7000
	s_addc_u32 s101, s101, 0
	global_load_dword v214, v248, s[100:101]
	s_add_u32 s100, s100, 0x7000
	s_addc_u32 s101, s101, 0
	global_load_dword v215, v248, s[100:101]
	s_add_u32 s100, s100, 0x7000
	s_addc_u32 s101, s101, 0
	global_load_dword v216, v248, s[100:101]
	s_add_u32 s100, s100, 0x7000
	s_addc_u32 s101, s101, 0
	global_load_dword v217, v248, s[100:101]
	s_add_u32 s100, s100, 0x7000
	s_addc_u32 s101, s101, 0
	global_load_dword v218, v248, s[100:101]
	s_add_u32 s100, s100, 0x7000
	s_addc_u32 s101, s101, 0
	global_load_dword v219, v248, s[100:101]
	s_add_u32 s100, s100, 0x7000
	s_addc_u32 s101, s101, 0
	global_load_dword v220, v248, s[100:101]
	s_add_u32 s100, s100, 0x7000
	s_addc_u32 s101, s101, 0
	global_load_dword v221, v248, s[100:101]
	s_add_u32 s100, s100, 0x7000
	s_addc_u32 s101, s101, 0
	global_load_dword v222, v248, s[100:101]
	s_add_u32 s100, s100, 0x7000
	s_addc_u32 s101, s101, 0
	global_load_dword v223, v248, s[100:101]
	s_add_u32 s100, s100, 0x7000
	s_addc_u32 s101, s101, 0
	global_load_dword v224, v248, s[100:101]
	s_add_u32 s100, s100, 0x7000
	s_addc_u32 s101, s101, 0
	global_load_dword v225, v248, s[100:101]
	s_add_u32 s100, s100, 0x7000
	s_addc_u32 s101, s101, 0
	global_load_dword v226, v248, s[100:101]
	s_add_u32 s100, s100, 0x7000
	s_addc_u32 s101, s101, 0
	global_load_dword v227, v248, s[100:101]
	s_add_u32 s100, s100, 0x7000
	s_addc_u32 s101, s101, 0
	global_load_dword v228, v248, s[100:101]
	s_add_u32 s100, s100, 0x7000
	s_addc_u32 s101, s101, 0
	global_load_dword v229, v248, s[100:101]
	s_add_u32 s100, s100, 0x7000
	s_addc_u32 s101, s101, 0
	global_load_dword v230, v248, s[100:101]
	s_add_u32 s100, s100, 0x7000
	s_addc_u32 s101, s101, 0
	global_load_dword v231, v248, s[100:101]
	s_add_u32 s100, s100, 0x7000
	s_addc_u32 s101, s101, 0
	global_load_dword v232, v248, s[100:101]
	s_add_u32 s100, s100, 0x7000
	s_addc_u32 s101, s101, 0
	global_load_dword v233, v248, s[100:101]
	s_add_u32 s100, s100, 0x7000
	s_addc_u32 s101, s101, 0
	global_load_dword v234, v248, s[100:101]
	s_add_u32 s100, s100, 0x7000
	s_addc_u32 s101, s101, 0
	global_load_dword v235, v248, s[100:101]
	s_add_u32 s100, s100, 0x7000
	s_addc_u32 s101, s101, 0
	global_load_dword v236, v248, s[100:101]
	s_add_u32 s100, s100, 0x7000
	s_addc_u32 s101, s101, 0
	global_load_dword v237, v248, s[100:101]
	s_add_u32 s100, s100, 0x7000
	s_addc_u32 s101, s101, 0
	global_load_dword v238, v248, s[100:101]
	s_add_u32 s100, s100, 0x7000
	s_addc_u32 s101, s101, 0
	global_load_dword v239, v248, s[100:101]
.Lp8f_s:
	v_cvt_f32_i32_e32 v126, v126
	v_cvt_f32_i32_e32 v127, v127
	v_cvt_f32_i32_e32 v128, v128
	v_cvt_f32_i32_e32 v129, v129
	v_cvt_f32_i32_e32 v122, v122
	v_cvt_f32_i32_e32 v141, v92
	v_cvt_f32_i32_e32 v92, v87
	v_cvt_f32_i32_e32 v87, v66
	v_cvt_f32_i32_e32 v66, v60
	v_cvt_f32_i32_e32 v60, v55
	v_cvt_f32_i32_e32 v55, v26
	v_cvt_f32_i32_e32 v26, v22
	v_cvt_f32_i32_e32 v22, v23
	v_cvt_f32_i32_e32 v23, v7
	v_cvt_f32_i32_e32 v7, v5
	v_fmamk_f32 v5, v126, 0xb80b6d22, v206
	v_cvt_f32_i32_e32 v123, v123
	v_cvt_f32_i32_e32 v136, v100
	v_cvt_f32_i32_e32 v100, v95
	v_cvt_f32_i32_e32 v95, v70
	v_cvt_f32_i32_e32 v70, v58
	v_cvt_f32_i32_e32 v58, v56
	v_cvt_f32_i32_e32 v56, v57
	v_cvt_f32_i32_e32 v57, v37
	v_cvt_f32_i32_e32 v37, v10
	v_cvt_f32_i32_e32 v10, v15
	v_exp_f32_e32 v5, v5
	v_fmamk_f32 v15, v127, 0xb80b6d22, v206
	v_cvt_f32_i32_e32 v124, v124
	v_cvt_f32_i32_e32 v143, v82
	v_cvt_f32_i32_e32 v82, v80
	v_cvt_f32_i32_e32 v80, v81
	v_cvt_f32_i32_e32 v81, v69
	v_cvt_f32_i32_e32 v69, v43
	v_cvt_f32_i32_e32 v43, v39
	v_cvt_f32_i32_e32 v39, v21
	v_cvt_f32_i32_e32 v21, v8
	v_cvt_f32_i32_e32 v8, v16
	v_exp_f32_e32 v15, v15
	v_fmamk_f32 v16, v128, 0xb80b6d22, v206
	v_cvt_f32_i32_e32 v125, v125
	v_cvt_f32_i32_e32 v139, v90
	v_cvt_f32_i32_e32 v90, v88
	v_cvt_f32_i32_e32 v88, v89
	v_cvt_f32_i32_e32 v89, v73
	v_cvt_f32_i32_e32 v73, v53
	v_cvt_f32_i32_e32 v53, v27
	v_cvt_f32_i32_e32 v27, v6
	v_cvt_f32_i32_e32 v6, v17
	v_exp_f32_e32 v16, v16
	v_fmamk_f32 v17, v129, 0xb80b6d22, v206
	v_cvt_f32_i32_e32 v142, v93
	v_cvt_f32_i32_e32 v93, v71
	v_cvt_f32_i32_e32 v71, v42
	v_cvt_f32_i32_e32 v42, v20
	v_cvt_f32_i32_e32 v20, v24
	v_exp_f32_e32 v17, v17
	v_fmamk_f32 v24, v122, 0xb80b6d22, v206
	v_cvt_f32_i32_e32 v114, v114
	v_cvt_f32_i32_e32 v138, v110
	v_cvt_f32_i32_e32 v110, v102
	v_cvt_f32_i32_e32 v102, v94
	v_cvt_f32_i32_e32 v94, v86
	v_cvt_f32_i32_e32 v86, v78
	v_cvt_f32_i32_e32 v78, v62
	v_cvt_f32_i32_e32 v62, v54
	v_cvt_f32_i32_e32 v54, v46
	v_cvt_f32_i32_e32 v46, v18
	v_cvt_f32_i32_e32 v18, v25
	v_add_f32_e32 v5, 0x4ce089af, v5
	v_exp_f32_e32 v24, v24
	v_fmamk_f32 v25, v123, 0xb80b6d22, v206
	v_cvt_f32_i32_e32 v115, v115
	v_cvt_f32_i32_e32 v133, v109
	v_cvt_f32_i32_e32 v109, v83
	v_cvt_f32_i32_e32 v83, v68
	v_cvt_f32_i32_e32 v68, v59
	v_cvt_f32_i32_e32 v59, v36
	v_cvt_f32_i32_e32 v36, v30
	v_cvt_f32_i32_e32 v30, v32
	v_rcp_f32_e32 v5, v5
;     __device__ __forceinline__ void operator()(const Acc& acc, const Unit& u, int wr, int wc, int fr, int fq) const {
;     ...
;             for (int m = 0; m < 4; ++m) { const size_t off = (size_t)(row0 + ai * HALF + m * 16) * ldc + col0;
;                 float h[8];
; #pragma unroll
;                 for (int n = 0; n < 2; ++n)
; #pragma unroll
;                     for (int e = 0; e < 4; ++e) { const float a0 = acc[ai][0][m][n][e], a1 = acc[ai][1][m][n][e];
;                         h[n * 4 + e] = (a0 * a1) * __builtin_amdgcn_rcpf(c3 + __builtin_amdgcn_exp2f(fmaf(a0, c1, c0))); }
;                 if constexpr (FP8OUT == 2) { u32x2 w; w.x = pk4_i8(h[0], h[1], h[2], h[3]); w.y = pk4_i8(h[4], h[5], h[6], h[7]); *(u32x2*)((unsigned char*)H + off) = w; }
	v_add_f32_e32 v15, 0x4ce089af, v15
	v_exp_f32_e32 v25, v25
	v_fmamk_f32 v32, v124, 0xb80b6d22, v206
	v_cvt_f32_i32_e32 v116, v116
	v_cvt_f32_i32_e32 v134, v98
	v_cvt_f32_i32_e32 v98, v96
	v_cvt_f32_i32_e32 v96, v97
	v_cvt_f32_i32_e32 v97, v77
	v_cvt_f32_i32_e32 v77, v51
	v_cvt_f32_i32_e32 v51, v28
	v_cvt_f32_i32_e32 v28, v33
	v_rcp_f32_e32 v15, v15
	v_add_f32_e32 v16, 0x4ce089af, v16
	v_exp_f32_e32 v32, v32
	v_fmamk_f32 v33, v125, 0xb80b6d22, v206
	v_cvt_f32_i32_e32 v117, v117
	v_rcp_f32_e32 v16, v16
	v_add_f32_e32 v17, 0x4ce089af, v17
	v_exp_f32_e32 v33, v33
	v_cvt_f32_i32_e32 v130, v106
	v_cvt_f32_i32_e32 v106, v104
	v_cvt_f32_i32_e32 v104, v105
	v_cvt_f32_i32_e32 v105, v85
	v_cvt_f32_i32_e32 v85, v67
	v_cvt_f32_i32_e32 v67, v44
	v_cvt_f32_i32_e32 v44, v19
	v_cvt_f32_i32_e32 v19, v9
	v_cvt_f32_i32_e32 v9, v4
	v_mul_f32_e32 v4, v114, v126
	v_rcp_f32_e32 v17, v17
	v_add_f32_e32 v24, 0x4ce089af, v24
	v_cvt_f32_i32_e32 v131, v107
	v_mul_f32_e32 v4, v5, v4
	v_mul_f32_e32 v5, v115, v127
	v_rcp_f32_e32 v24, v24
	v_add_f32_e32 v25, 0x4ce089af, v25
	v_cvt_f32_i32_e32 v132, v108
	v_mul_f32_e32 v5, v15, v5
	v_mul_f32_e32 v15, v116, v128
	v_rcp_f32_e32 v25, v25
	v_add_f32_e32 v32, 0x4ce089af, v32
	v_mul_f32_e32 v15, v16, v15
	v_mul_f32_e32 v16, v117, v129
	v_rcp_f32_e32 v32, v32
	v_add_f32_e32 v33, 0x4ce089af, v33
	v_mul_f32_e32 v16, v17, v16
	v_mul_f32_e32 v17, v130, v122
	v_rcp_f32_e32 v33, v33
	v_mul_f32_e32 v17, v24, v17
	v_mul_f32_e32 v24, v131, v123
	v_mul_f32_e32 v24, v25, v24
	v_mul_f32_e32 v25, v132, v124
	v_med3_f32 v4, v4, s1, v207
	v_med3_f32 v5, v5, s1, v207
	v_med3_f32 v15, v15, s1, v207
	v_med3_f32 v16, v16, s1, v207
	v_mul_f32_e32 v25, v32, v25
	v_mul_f32_e32 v32, v133, v125
	v_add_f32_e32 v4, 0x4b400000, v4
	v_add_f32_e32 v5, 0x4b400000, v5
	v_add_f32_e32 v15, 0x4b400000, v15
	v_add_f32_e32 v16, 0x4b400000, v16
	v_mul_f32_e32 v32, v33, v32
	v_perm_b32 v4, v5, v4, s33
	v_perm_b32 v5, v16, v15, s33
	v_perm_b32 v16, v5, v4, s87
	v_med3_f32 v4, v17, s1, v207
	v_med3_f32 v5, v24, s1, v207
	v_med3_f32 v15, v25, s1, v207
	v_med3_f32 v17, v32, s1, v207
	v_add_f32_e32 v4, 0x4b400000, v4
	v_add_f32_e32 v5, 0x4b400000, v5
	v_add_f32_e32 v15, 0x4b400000, v15
	v_add_f32_e32 v17, 0x4b400000, v17
	v_cvt_f32_i32_e32 v118, v118
	v_perm_b32 v4, v5, v4, s33
	v_perm_b32 v5, v17, v15, s33
	v_cvt_f32_i32_e32 v119, v119
	v_cvt_f32_i32_e32 v135, v99
	v_cvt_f32_i32_e32 v107, v84
	v_cvt_f32_i32_e32 v99, v76
	v_cvt_f32_i32_e32 v84, v79
	v_cvt_f32_i32_e32 v79, v50
	v_cvt_f32_i32_e32 v76, v63
	v_cvt_f32_i32_e32 v63, v34
	v_cvt_f32_i32_e32 v50, v48
	v_cvt_f32_i32_e32 v48, v29
	v_cvt_f32_i32_e32 v34, v31
	v_cvt_f32_i32_e32 v31, v12
	v_cvt_f32_i32_e32 v29, v13
	v_cvt_f32_i32_e32 v12, v14
	v_cvt_f32_i32_e32 v13, v2
	v_lshl_add_u32 v14, s56, 8, v186
	v_lshl_or_b32 v2, s57, 7, v203
	v_perm_b32 v17, v5, v4, s87
	v_mov_b64_e32 v[4:5], s[36:37]
	v_cvt_f32_i32_e32 v120, v120
	v_cvt_f32_i32_e32 v108, v103
	v_cvt_f32_i32_e32 v103, v74
	v_cvt_f32_i32_e32 v74, v64
	v_cvt_f32_i32_e32 v64, v61
	v_cvt_f32_i32_e32 v61, v35
	v_cvt_f32_i32_e32 v35, v11
	v_cvt_f32_i32_e32 v11, v3
	v_ashrrev_i32_e32 v3, 31, v2
	v_mad_i64_i32 v[24:25], s[8:9], v14, s88, v[4:5]
	v_cvt_f32_i32_e32 v121, v121
	v_lshl_add_u64 v[24:25], v[24:25], 0, v[2:3]
	global_store_dwordx2 v[24:25], v[16:17], off
	v_fmamk_f32 v17, v118, 0xb80b6d22, v206
	v_exp_f32_e32 v17, v17
	v_fmamk_f32 v24, v119, 0xb80b6d22, v206
	v_exp_f32_e32 v24, v24
	v_fmamk_f32 v25, v120, 0xb80b6d22, v206
	v_exp_f32_e32 v25, v25
	v_fmamk_f32 v32, v121, 0xb80b6d22, v206
	v_exp_f32_e32 v32, v32
	v_fmamk_f32 v33, v138, 0xb80b6d22, v206
	v_add_f32_e32 v17, 0x4ce089af, v17
	v_exp_f32_e32 v33, v33
	v_rcp_f32_e32 v17, v17
	v_add_f32_e32 v24, 0x4ce089af, v24
	v_rcp_f32_e32 v24, v24
	v_add_f32_e32 v25, 0x4ce089af, v25
	v_cvt_f32_i32_e32 v137, v101
	v_cvt_f32_i32_e32 v111, v111
	v_rcp_f32_e32 v25, v25
	v_add_f32_e32 v32, 0x4ce089af, v32
	v_cvt_f32_i32_e32 v112, v112
	v_mul_f32_e32 v16, v134, v118
	v_rcp_f32_e32 v32, v32
	v_add_f32_e32 v33, 0x4ce089af, v33
	v_cvt_f32_i32_e32 v140, v91
	v_cvt_f32_i32_e32 v113, v113
	v_mul_f32_e32 v16, v17, v16
	v_mul_f32_e32 v17, v135, v119
	v_rcp_f32_e32 v33, v33
	v_mul_f32_e32 v17, v24, v17
	v_mul_f32_e32 v24, v136, v120
	v_cvt_f32_i32_e32 v91, v72
	v_cvt_f32_i32_e32 v72, v65
	v_cvt_f32_i32_e32 v65, v45
	v_cvt_f32_i32_e32 v45, v38
	v_cvt_f32_i32_e32 v38, v41
	v_mul_f32_e32 v24, v25, v24
	v_mul_f32_e32 v25, v137, v121
	v_fmamk_f32 v41, v111, 0xb80b6d22, v206
	v_cvt_f32_i32_e32 v101, v75
	v_cvt_f32_i32_e32 v75, v52
	v_cvt_f32_i32_e32 v52, v47
	v_cvt_f32_i32_e32 v47, v49
	v_mul_f32_e32 v25, v32, v25
	v_mul_f32_e32 v32, v139, v138
	v_exp_f32_e32 v41, v41
	v_fmamk_f32 v49, v112, 0xb80b6d22, v206
	v_mul_f32_e32 v32, v33, v32
	v_mul_f32_e32 v33, v140, v111
	v_exp_f32_e32 v49, v49
	v_fmamk_f32 v111, v113, 0xb80b6d22, v206
	v_exp_f32_e32 v111, v111
	v_add_f32_e32 v41, 0x4ce089af, v41
	v_rcp_f32_e32 v41, v41
	v_add_f32_e32 v49, 0x4ce089af, v49
	v_rcp_f32_e32 v49, v49
	v_add_f32_e32 v111, 0x4ce089af, v111
	v_rcp_f32_e32 v111, v111
	v_mul_f32_e32 v33, v41, v33
	v_mul_f32_e32 v41, v141, v112
	v_med3_f32 v16, v16, s1, v207
	v_med3_f32 v17, v17, s1, v207
	v_med3_f32 v24, v24, s1, v207
	v_med3_f32 v25, v25, s1, v207
	v_mul_f32_e32 v41, v49, v41
	v_mul_f32_e32 v49, v142, v113
	v_add_f32_e32 v16, 0x4b400000, v16
	v_add_f32_e32 v17, 0x4b400000, v17
	v_add_f32_e32 v24, 0x4b400000, v24
	v_add_f32_e32 v25, 0x4b400000, v25
	v_mul_f32_e32 v49, v111, v49
	v_perm_b32 v16, v17, v16, s33
	v_perm_b32 v17, v25, v24, s33
	v_perm_b32 v16, v17, v16, s87
	v_med3_f32 v17, v32, s1, v207
	v_med3_f32 v24, v33, s1, v207
	v_med3_f32 v25, v41, s1, v207
;     __device__ __forceinline__ void operator()(const Acc& acc, const Unit& u, int wr, int wc, int fr, int fq) const {
;     ...
;             for (int m = 0; m < 4; ++m) { const size_t off = (size_t)(row0 + ai * HALF + m * 16) * ldc + col0;
;                 float h[8];
; #pragma unroll
;                 for (int n = 0; n < 2; ++n)
; #pragma unroll
;                     for (int e = 0; e < 4; ++e) { const float a0 = acc[ai][0][m][n][e], a1 = acc[ai][1][m][n][e];
;                         h[n * 4 + e] = (a0 * a1) * __builtin_amdgcn_rcpf(c3 + __builtin_amdgcn_exp2f(fmaf(a0, c1, c0))); }
;                 if constexpr (FP8OUT == 2) { u32x2 w; w.x = pk4_i8(h[0], h[1], h[2], h[3]); w.y = pk4_i8(h[4], h[5], h[6], h[7]); *(u32x2*)((unsigned char*)H + off) = w; }
	v_med3_f32 v32, v49, s1, v207
	v_add_f32_e32 v17, 0x4b400000, v17
	v_add_f32_e32 v24, 0x4b400000, v24
	v_add_f32_e32 v25, 0x4b400000, v25
	v_add_f32_e32 v32, 0x4b400000, v32
	v_or_b32_e32 v15, 16, v14
	v_perm_b32 v17, v24, v17, s33
	v_perm_b32 v24, v32, v25, s33
	v_perm_b32 v17, v24, v17, s87
	v_mad_i64_i32 v[24:25], s[8:9], v15, s88, v[4:5]
	v_lshl_add_u64 v[24:25], v[24:25], 0, v[2:3]
	global_store_dwordx2 v[24:25], v[16:17], off
	v_fmamk_f32 v17, v110, 0xb80b6d22, v206
	v_exp_f32_e32 v17, v17
	v_fmamk_f32 v24, v108, 0xb80b6d22, v206
	v_exp_f32_e32 v24, v24
	v_fmamk_f32 v25, v106, 0xb80b6d22, v206
	v_exp_f32_e32 v25, v25
	v_fmamk_f32 v32, v104, 0xb80b6d22, v206
	v_exp_f32_e32 v32, v32
	v_fmamk_f32 v33, v102, 0xb80b6d22, v206
	v_add_f32_e32 v17, 0x4ce089af, v17
	v_exp_f32_e32 v33, v33
	v_fmamk_f32 v41, v100, 0xb80b6d22, v206
	v_rcp_f32_e32 v17, v17
	v_add_f32_e32 v24, 0x4ce089af, v24
	v_exp_f32_e32 v41, v41
	v_fmamk_f32 v49, v98, 0xb80b6d22, v206
	v_rcp_f32_e32 v24, v24
	v_add_f32_e32 v25, 0x4ce089af, v25
	v_exp_f32_e32 v49, v49
	v_rcp_f32_e32 v25, v25
	v_add_f32_e32 v32, 0x4ce089af, v32
	v_mul_f32_e32 v16, v143, v110
	v_rcp_f32_e32 v32, v32
	v_add_f32_e32 v33, 0x4ce089af, v33
	v_mul_f32_e32 v16, v17, v16
	v_mul_f32_e32 v17, v109, v108
	v_rcp_f32_e32 v33, v33
	v_add_f32_e32 v41, 0x4ce089af, v41
	v_mul_f32_e32 v17, v24, v17
	v_mul_f32_e32 v24, v107, v106
	v_rcp_f32_e32 v41, v41
	v_add_f32_e32 v49, 0x4ce089af, v49
	v_mul_f32_e32 v24, v25, v24
	v_mul_f32_e32 v25, v105, v104
	v_rcp_f32_e32 v49, v49
	v_mul_f32_e32 v25, v32, v25
	v_mul_f32_e32 v32, v103, v102
	v_mul_f32_e32 v32, v33, v32
	v_mul_f32_e32 v33, v101, v100
	v_mul_f32_e32 v33, v41, v33
	v_mul_f32_e32 v41, v99, v98
	v_mul_f32_e32 v41, v49, v41
	v_mul_f32_e32 v49, v97, v96
	v_fmamk_f32 v96, v96, 0xb80b6d22, v206
	v_exp_f32_e32 v96, v96
	v_med3_f32 v16, v16, s1, v207
	v_med3_f32 v17, v17, s1, v207
	v_med3_f32 v24, v24, s1, v207
	v_add_f32_e32 v96, 0x4ce089af, v96
	v_rcp_f32_e32 v96, v96
	v_med3_f32 v25, v25, s1, v207
	v_add_f32_e32 v16, 0x4b400000, v16
	v_add_f32_e32 v17, 0x4b400000, v17
	v_add_f32_e32 v24, 0x4b400000, v24
	v_add_f32_e32 v25, 0x4b400000, v25
	v_mul_f32_e32 v49, v96, v49
	v_perm_b32 v16, v17, v16, s33
	v_perm_b32 v17, v25, v24, s33
	v_perm_b32 v16, v17, v16, s87
	v_med3_f32 v17, v32, s1, v207
	v_med3_f32 v24, v33, s1, v207
	v_med3_f32 v25, v41, s1, v207
	v_med3_f32 v32, v49, s1, v207
	v_add_f32_e32 v17, 0x4b400000, v17
	v_add_f32_e32 v24, 0x4b400000, v24
	v_add_f32_e32 v25, 0x4b400000, v25
	v_add_f32_e32 v32, 0x4b400000, v32
	v_or_b32_e32 v15, 32, v14
	v_perm_b32 v17, v24, v17, s33
	v_perm_b32 v24, v32, v25, s33
	v_perm_b32 v17, v24, v17, s87
	v_mad_i64_i32 v[24:25], s[8:9], v15, s88, v[4:5]
	v_lshl_add_u64 v[24:25], v[24:25], 0, v[2:3]
	global_store_dwordx2 v[24:25], v[16:17], off
	v_fmamk_f32 v17, v94, 0xb80b6d22, v206
	v_exp_f32_e32 v17, v17
	v_fmamk_f32 v24, v92, 0xb80b6d22, v206
	v_exp_f32_e32 v24, v24
	v_fmamk_f32 v25, v90, 0xb80b6d22, v206
	v_exp_f32_e32 v25, v25
	v_fmamk_f32 v32, v88, 0xb80b6d22, v206
	v_exp_f32_e32 v32, v32
	v_fmamk_f32 v33, v86, 0xb80b6d22, v206
	v_add_f32_e32 v17, 0x4ce089af, v17
	v_exp_f32_e32 v33, v33
	v_fmamk_f32 v41, v84, 0xb80b6d22, v206
	v_rcp_f32_e32 v17, v17
	v_add_f32_e32 v24, 0x4ce089af, v24
	v_exp_f32_e32 v41, v41
	v_fmamk_f32 v49, v82, 0xb80b6d22, v206
	v_rcp_f32_e32 v24, v24
	v_add_f32_e32 v25, 0x4ce089af, v25
	v_exp_f32_e32 v49, v49
	v_rcp_f32_e32 v25, v25
	v_add_f32_e32 v32, 0x4ce089af, v32
	v_mul_f32_e32 v16, v95, v94
	v_rcp_f32_e32 v32, v32
	v_add_f32_e32 v33, 0x4ce089af, v33
	v_mul_f32_e32 v16, v17, v16
	v_mul_f32_e32 v17, v93, v92
	v_rcp_f32_e32 v33, v33
	v_add_f32_e32 v41, 0x4ce089af, v41
	v_mul_f32_e32 v17, v24, v17
	v_mul_f32_e32 v24, v91, v90
	v_rcp_f32_e32 v41, v41
	v_add_f32_e32 v49, 0x4ce089af, v49
	v_mul_f32_e32 v24, v25, v24
	v_mul_f32_e32 v25, v89, v88
	v_rcp_f32_e32 v49, v49
	v_mul_f32_e32 v25, v32, v25
	v_mul_f32_e32 v32, v87, v86
	v_mul_f32_e32 v32, v33, v32
	v_mul_f32_e32 v33, v85, v84
	v_mul_f32_e32 v33, v41, v33
	v_mul_f32_e32 v41, v83, v82
	v_mul_f32_e32 v41, v49, v41
	v_mul_f32_e32 v49, v81, v80
	v_fmamk_f32 v80, v80, 0xb80b6d22, v206
	v_exp_f32_e32 v80, v80
	v_med3_f32 v16, v16, s1, v207
	v_med3_f32 v17, v17, s1, v207
	v_med3_f32 v24, v24, s1, v207
	v_add_f32_e32 v80, 0x4ce089af, v80
	v_rcp_f32_e32 v80, v80
	v_med3_f32 v25, v25, s1, v207
	v_add_f32_e32 v16, 0x4b400000, v16
	v_add_f32_e32 v17, 0x4b400000, v17
	v_add_f32_e32 v24, 0x4b400000, v24
	v_add_f32_e32 v25, 0x4b400000, v25
	v_mul_f32_e32 v49, v80, v49
	v_perm_b32 v16, v17, v16, s33
	v_perm_b32 v17, v25, v24, s33
	v_perm_b32 v16, v17, v16, s87
	v_med3_f32 v17, v32, s1, v207
	v_med3_f32 v24, v33, s1, v207
	v_med3_f32 v25, v41, s1, v207
	v_med3_f32 v32, v49, s1, v207
	v_add_f32_e32 v17, 0x4b400000, v17
	v_add_f32_e32 v24, 0x4b400000, v24
	v_add_f32_e32 v25, 0x4b400000, v25
	v_add_f32_e32 v32, 0x4b400000, v32
	v_or_b32_e32 v15, 48, v14
	v_perm_b32 v17, v24, v17, s33
	v_perm_b32 v24, v32, v25, s33
	v_perm_b32 v17, v24, v17, s87
	v_mad_i64_i32 v[24:25], s[8:9], v15, s88, v[4:5]
	v_lshl_add_u64 v[24:25], v[24:25], 0, v[2:3]
	global_store_dwordx2 v[24:25], v[16:17], off
	s_cmp_lt_u32 s98, 28
	s_cbranch_scc0 .Lp8f_m
; template <int MODE>
; __device__ __forceinline__ void tr_matrix6(const float* W, int nb, int K, int N, unsigned char* WT, int drows, int rot, int gw, int NGW, int lane, float wscale) {
;     ...
;         const int drow0 = (MODE == 0) ? n0 : ((n0 >> 7) * 256 + (n0 & 127) + (MODE == 2 ? 128 : 0));
;         unsigned char* dst = WT + (size_t)e * drows * K + (size_t)(drow0 + 4 * c) * K + k0 + 32 * q;
; #pragma unroll
;         for (int j = 0; j < 4; ++j) { float x[32];
; #pragma unroll
;             for (int i = 0; i < 32; ++i) x[i] = v[i][j] * wscale;
;             const v6u w = pk32_fp6(x);
;             *(u32x4*)(dst + (size_t)j * K) = (u32x4){w[0], w[1], w[2], w[3]}; *(u32x4*)(dst + (size_t)j * K + 16) = (u32x4){w[4], w[5], 0u, 0u}; }
	s_waitcnt vmcnt(4)
	v_mul_f32_e32 v208, 0x42b40000, v208
	v_mul_f32_e32 v209, 0x42b40000, v209
	v_mul_f32_e32 v210, 0x42b40000, v210
	v_mul_f32_e32 v211, 0x42b40000, v211
	v_mul_f32_e32 v212, 0x42b40000, v212
	v_mul_f32_e32 v213, 0x42b40000, v213
	v_mul_f32_e32 v214, 0x42b40000, v214
	v_mul_f32_e32 v215, 0x42b40000, v215
	v_mul_f32_e32 v216, 0x42b40000, v216
	v_mul_f32_e32 v217, 0x42b40000, v217
	v_mul_f32_e32 v218, 0x42b40000, v218
	v_mul_f32_e32 v219, 0x42b40000, v219
	v_mul_f32_e32 v220, 0x42b40000, v220
	v_mul_f32_e32 v221, 0x42b40000, v221
	v_mul_f32_e32 v222, 0x42b40000, v222
	v_mul_f32_e32 v223, 0x42b40000, v223
	v_mul_f32_e32 v224, 0x42b40000, v224
	v_mul_f32_e32 v225, 0x42b40000, v225
	v_mul_f32_e32 v226, 0x42b40000, v226
	v_mul_f32_e32 v227, 0x42b40000, v227
	v_mul_f32_e32 v228, 0x42b40000, v228
	v_mul_f32_e32 v229, 0x42b40000, v229
	v_mul_f32_e32 v230, 0x42b40000, v230
	v_mul_f32_e32 v231, 0x42b40000, v231
	v_mul_f32_e32 v232, 0x42b40000, v232
	v_mul_f32_e32 v233, 0x42b40000, v233
	v_mul_f32_e32 v234, 0x42b40000, v234
	v_mul_f32_e32 v235, 0x42b40000, v235
	v_mul_f32_e32 v236, 0x42b40000, v236
	v_mul_f32_e32 v237, 0x42b40000, v237
	v_mul_f32_e32 v238, 0x42b40000, v238
	v_mul_f32_e32 v239, 0x42b40000, v239
	v_med3_f32 v208, v208, v255, v254
	v_med3_f32 v209, v209, v255, v254
	v_med3_f32 v210, v210, v255, v254
	v_med3_f32 v211, v211, v255, v254
	v_med3_f32 v212, v212, v255, v254
	v_med3_f32 v213, v213, v255, v254
	v_med3_f32 v214, v214, v255, v254
	v_med3_f32 v215, v215, v255, v254
	v_med3_f32 v216, v216, v255, v254
	v_med3_f32 v217, v217, v255, v254
	v_med3_f32 v218, v218, v255, v254
	v_med3_f32 v219, v219, v255, v254
	v_med3_f32 v220, v220, v255, v254
	v_med3_f32 v221, v221, v255, v254
	v_med3_f32 v222, v222, v255, v254
	v_med3_f32 v223, v223, v255, v254
	v_med3_f32 v224, v224, v255, v254
	v_med3_f32 v225, v225, v255, v254
	v_med3_f32 v226, v226, v255, v254
	v_med3_f32 v227, v227, v255, v254
	v_med3_f32 v228, v228, v255, v254
	v_med3_f32 v229, v229, v255, v254
	v_med3_f32 v230, v230, v255, v254
	v_med3_f32 v231, v231, v255, v254
	v_med3_f32 v232, v232, v255, v254
	v_med3_f32 v233, v233, v255, v254
	v_med3_f32 v234, v234, v255, v254
	v_med3_f32 v235, v235, v255, v254
	v_med3_f32 v236, v236, v255, v254
	v_med3_f32 v237, v237, v255, v254
	v_med3_f32 v238, v238, v255, v254
	v_med3_f32 v239, v239, v255, v254
	v_cvt_scalef32_2xpk16_fp6_f32 v[240:245], v[208:223], v[224:239], 1.0
	v_readlane_b32 s100, v252, 6
	v_readlane_b32 s101, v252, 7
	s_lshr_b32 s99, s98, 1
	s_lshl_b32 s99, s99, 19
	s_add_u32 s100, s100, s99
	s_addc_u32 s101, s101, 0
	s_and_b32 s99, s98, 1
	s_lshl_b32 s99, s99, 17
	s_add_u32 s100, s100, s99
	s_addc_u32 s101, s101, 0
	global_store_dwordx4 v249, v[240:243], s[100:101]
	global_store_dwordx4 v249, v[244:247], s[100:101] offset:16
	s_add_i32 s98, s98, 1
	s_cmp_lt_u32 s98, 28
	s_cbranch_scc0 .Lp8f_m
	v_readlane_b32 s100, v252, 4
	v_readlane_b32 s101, v252, 5
	s_lshl_b32 s99, s98, 8
	s_nop 1
	s_add_u32 s100, s100, s99
	s_addc_u32 s101, s101, 0
	global_load_dword v208, v248, s[100:101]
	s_add_u32 s100, s100, 0x7000
	s_addc_u32 s101, s101, 0
	global_load_dword v209, v248, s[100:101]
	s_add_u32 s100, s100, 0x7000
	s_addc_u32 s101, s101, 0
	global_load_dword v210, v248, s[100:101]
	s_add_u32 s100, s100, 0x7000
	s_addc_u32 s101, s101, 0
	global_load_dword v211, v248, s[100:101]
	s_add_u32 s100, s100, 0x7000
	s_addc_u32 s101, s101, 0
	global_load_dword v212, v248, s[100:101]
	s_add_u32 s100, s100, 0x7000
	s_addc_u32 s101, s101, 0
	global_load_dword v213, v248, s[100:101]
	s_add_u32 s100, s100, 0x7000
	s_addc_u32 s101, s101, 0
	global_load_dword v214, v248, s[100:101]
	s_add_u32 s100, s100, 0x7000
	s_addc_u32 s101, s101, 0
	global_load_dword v215, v248, s[100:101]
	s_add_u32 s100, s100, 0x7000
	s_addc_u32 s101, s101, 0
	global_load_dword v216, v248, s[100:101]
	s_add_u32 s100, s100, 0x7000
	s_addc_u32 s101, s101, 0
	global_load_dword v217, v248, s[100:101]
	s_add_u32 s100, s100, 0x7000
	s_addc_u32 s101, s101, 0
	global_load_dword v218, v248, s[100:101]
	s_add_u32 s100, s100, 0x7000
	s_addc_u32 s101, s101, 0
	global_load_dword v219, v248, s[100:101]
	s_add_u32 s100, s100, 0x7000
	s_addc_u32 s101, s101, 0
	global_load_dword v220, v248, s[100:101]
	s_add_u32 s100, s100, 0x7000
	s_addc_u32 s101, s101, 0
	global_load_dword v221, v248, s[100:101]
	s_add_u32 s100, s100, 0x7000
	s_addc_u32 s101, s101, 0
	global_load_dword v222, v248, s[100:101]
	s_add_u32 s100, s100, 0x7000
	s_addc_u32 s101, s101, 0
	global_load_dword v223, v248, s[100:101]
	s_add_u32 s100, s100, 0x7000
	s_addc_u32 s101, s101, 0
	global_load_dword v224, v248, s[100:101]
	s_add_u32 s100, s100, 0x7000
	s_addc_u32 s101, s101, 0
	global_load_dword v225, v248, s[100:101]
	s_add_u32 s100, s100, 0x7000
	s_addc_u32 s101, s101, 0
	global_load_dword v226, v248, s[100:101]
	s_add_u32 s100, s100, 0x7000
	s_addc_u32 s101, s101, 0
	global_load_dword v227, v248, s[100:101]
	s_add_u32 s100, s100, 0x7000
	s_addc_u32 s101, s101, 0
	global_load_dword v228, v248, s[100:101]
	s_add_u32 s100, s100, 0x7000
	s_addc_u32 s101, s101, 0
	global_load_dword v229, v248, s[100:101]
	s_add_u32 s100, s100, 0x7000
	s_addc_u32 s101, s101, 0
	global_load_dword v230, v248, s[100:101]
	s_add_u32 s100, s100, 0x7000
	s_addc_u32 s101, s101, 0
	global_load_dword v231, v248, s[100:101]
	s_add_u32 s100, s100, 0x7000
	s_addc_u32 s101, s101, 0
	global_load_dword v232, v248, s[100:101]
	s_add_u32 s100, s100, 0x7000
	s_addc_u32 s101, s101, 0
	global_load_dword v233, v248, s[100:101]
	s_add_u32 s100, s100, 0x7000
	s_addc_u32 s101, s101, 0
	global_load_dword v234, v248, s[100:101]
	s_add_u32 s100, s100, 0x7000
	s_addc_u32 s101, s101, 0
	global_load_dword v235, v248, s[100:101]
	s_add_u32 s100, s100, 0x7000
	s_addc_u32 s101, s101, 0
	global_load_dword v236, v248, s[100:101]
	s_add_u32 s100, s100, 0x7000
	s_addc_u32 s101, s101, 0
	global_load_dword v237, v248, s[100:101]
	s_add_u32 s100, s100, 0x7000
	s_addc_u32 s101, s101, 0
	global_load_dword v238, v248, s[100:101]
	s_add_u32 s100, s100, 0x7000
	s_addc_u32 s101, s101, 0
	global_load_dword v239, v248, s[100:101]
;     __device__ __forceinline__ void operator()(const Acc& acc, const Unit& u, int wr, int wc, int fr, int fq) const {
;     ...
;             for (int m = 0; m < 4; ++m) { const size_t off = (size_t)(row0 + ai * HALF + m * 16) * ldc + col0;
;                 float h[8];
; #pragma unroll
;                 for (int n = 0; n < 2; ++n)
; #pragma unroll
;                     for (int e = 0; e < 4; ++e) { const float a0 = acc[ai][0][m][n][e], a1 = acc[ai][1][m][n][e];
;                         h[n * 4 + e] = (a0 * a1) * __builtin_amdgcn_rcpf(c3 + __builtin_amdgcn_exp2f(fmaf(a0, c1, c0))); }
;                 if constexpr (FP8OUT == 2) { u32x2 w; w.x = pk4_i8(h[0], h[1], h[2], h[3]); w.y = pk4_i8(h[4], h[5], h[6], h[7]); *(u32x2*)((unsigned char*)H + off) = w; }
.Lp8f_m:
	v_fmamk_f32 v17, v78, 0xb80b6d22, v206
	v_exp_f32_e32 v17, v17
	v_fmamk_f32 v24, v76, 0xb80b6d22, v206
	v_exp_f32_e32 v24, v24
	v_fmamk_f32 v25, v74, 0xb80b6d22, v206
	v_exp_f32_e32 v25, v25
	v_fmamk_f32 v32, v72, 0xb80b6d22, v206
	v_exp_f32_e32 v32, v32
	v_fmamk_f32 v33, v70, 0xb80b6d22, v206
	v_add_f32_e32 v17, 0x4ce089af, v17
	v_exp_f32_e32 v33, v33
	v_fmamk_f32 v41, v68, 0xb80b6d22, v206
	v_rcp_f32_e32 v17, v17
	v_add_f32_e32 v24, 0x4ce089af, v24
	v_exp_f32_e32 v41, v41
	v_fmamk_f32 v49, v66, 0xb80b6d22, v206
	v_rcp_f32_e32 v24, v24
	v_add_f32_e32 v25, 0x4ce089af, v25
	v_exp_f32_e32 v49, v49
	v_rcp_f32_e32 v25, v25
	v_add_f32_e32 v32, 0x4ce089af, v32
	v_mul_f32_e32 v16, v79, v78
	v_rcp_f32_e32 v32, v32
	v_add_f32_e32 v33, 0x4ce089af, v33
	v_mul_f32_e32 v16, v17, v16
	v_mul_f32_e32 v17, v77, v76
	v_rcp_f32_e32 v33, v33
	v_add_f32_e32 v41, 0x4ce089af, v41
	v_mul_f32_e32 v17, v24, v17
	v_mul_f32_e32 v24, v75, v74
	v_rcp_f32_e32 v41, v41
	v_add_f32_e32 v49, 0x4ce089af, v49
	v_mul_f32_e32 v24, v25, v24
	v_mul_f32_e32 v25, v73, v72
	v_rcp_f32_e32 v49, v49
	v_mul_f32_e32 v25, v32, v25
	v_mul_f32_e32 v32, v71, v70
	v_mul_f32_e32 v32, v33, v32
	v_mul_f32_e32 v33, v69, v68
	v_mul_f32_e32 v33, v41, v33
	v_mul_f32_e32 v41, v67, v66
	v_mul_f32_e32 v41, v49, v41
	v_mul_f32_e32 v49, v65, v64
	v_fmamk_f32 v64, v64, 0xb80b6d22, v206
	v_exp_f32_e32 v64, v64
	v_med3_f32 v16, v16, s1, v207
	v_med3_f32 v17, v17, s1, v207
	v_med3_f32 v24, v24, s1, v207
	v_add_f32_e32 v64, 0x4ce089af, v64
	v_rcp_f32_e32 v64, v64
	v_med3_f32 v25, v25, s1, v207
	v_add_f32_e32 v16, 0x4b400000, v16
	v_add_f32_e32 v17, 0x4b400000, v17
	v_add_f32_e32 v24, 0x4b400000, v24
	v_add_f32_e32 v25, 0x4b400000, v25
	v_mul_f32_e32 v49, v64, v49
	v_perm_b32 v16, v17, v16, s33
	v_perm_b32 v17, v25, v24, s33
	v_perm_b32 v16, v17, v16, s87
	v_med3_f32 v17, v32, s1, v207
	v_med3_f32 v24, v33, s1, v207
	v_med3_f32 v25, v41, s1, v207
	v_med3_f32 v32, v49, s1, v207
	v_add_f32_e32 v17, 0x4b400000, v17
	v_add_f32_e32 v24, 0x4b400000, v24
	v_add_f32_e32 v25, 0x4b400000, v25
	v_add_f32_e32 v32, 0x4b400000, v32
	v_add_u32_e32 v15, 0x80, v14
	v_perm_b32 v17, v24, v17, s33
	v_perm_b32 v24, v32, v25, s33
	v_perm_b32 v17, v24, v17, s87
	v_mad_i64_i32 v[24:25], s[8:9], v15, s88, v[4:5]
	v_lshl_add_u64 v[24:25], v[24:25], 0, v[2:3]
	global_store_dwordx2 v[24:25], v[16:17], off
	v_fmamk_f32 v17, v62, 0xb80b6d22, v206
	v_exp_f32_e32 v17, v17
	v_fmamk_f32 v24, v60, 0xb80b6d22, v206
	v_exp_f32_e32 v24, v24
	v_fmamk_f32 v25, v58, 0xb80b6d22, v206
	v_exp_f32_e32 v25, v25
	v_fmamk_f32 v32, v56, 0xb80b6d22, v206
	v_exp_f32_e32 v32, v32
	v_fmamk_f32 v33, v54, 0xb80b6d22, v206
	v_add_f32_e32 v17, 0x4ce089af, v17
	v_exp_f32_e32 v33, v33
	v_fmamk_f32 v41, v52, 0xb80b6d22, v206
	v_rcp_f32_e32 v17, v17
	v_add_f32_e32 v24, 0x4ce089af, v24
	v_exp_f32_e32 v41, v41
	v_fmamk_f32 v49, v50, 0xb80b6d22, v206
	v_mul_f32_e32 v48, v48, v47
	v_fmamk_f32 v47, v47, 0xb80b6d22, v206
	v_rcp_f32_e32 v24, v24
	v_add_f32_e32 v25, 0x4ce089af, v25
	v_exp_f32_e32 v49, v49
	v_exp_f32_e32 v47, v47
	v_rcp_f32_e32 v25, v25
	v_add_f32_e32 v32, 0x4ce089af, v32
	v_mul_f32_e32 v16, v63, v62
	v_rcp_f32_e32 v32, v32
	v_add_f32_e32 v33, 0x4ce089af, v33
	v_mul_f32_e32 v16, v17, v16
	v_mul_f32_e32 v17, v61, v60
	v_rcp_f32_e32 v33, v33
	v_add_f32_e32 v41, 0x4ce089af, v41
	v_mul_f32_e32 v17, v24, v17
	v_mul_f32_e32 v24, v59, v58
	v_rcp_f32_e32 v41, v41
	v_add_f32_e32 v49, 0x4ce089af, v49
	v_add_f32_e32 v47, 0x4ce089af, v47
	v_mul_f32_e32 v24, v25, v24
	v_mul_f32_e32 v25, v57, v56
	v_rcp_f32_e32 v49, v49
	v_rcp_f32_e32 v47, v47
	v_mul_f32_e32 v25, v32, v25
	v_mul_f32_e32 v32, v55, v54
	v_mul_f32_e32 v32, v33, v32
	v_mul_f32_e32 v33, v53, v52
	v_med3_f32 v16, v16, s1, v207
	v_med3_f32 v17, v17, s1, v207
	v_med3_f32 v24, v24, s1, v207
	v_med3_f32 v25, v25, s1, v207
	v_mul_f32_e32 v33, v41, v33
	v_mul_f32_e32 v41, v51, v50
	v_add_f32_e32 v16, 0x4b400000, v16
	v_add_f32_e32 v17, 0x4b400000, v17
	v_add_f32_e32 v24, 0x4b400000, v24
	v_add_f32_e32 v25, 0x4b400000, v25
	v_mul_f32_e32 v41, v49, v41
	v_mul_f32_e32 v47, v47, v48
	v_perm_b32 v16, v17, v16, s33
	v_perm_b32 v17, v25, v24, s33
	v_perm_b32 v16, v17, v16, s87
	v_med3_f32 v17, v32, s1, v207
	v_med3_f32 v24, v33, s1, v207
	v_med3_f32 v25, v41, s1, v207
	v_med3_f32 v32, v47, s1, v207
	v_add_f32_e32 v17, 0x4b400000, v17
	v_add_f32_e32 v24, 0x4b400000, v24
	v_add_f32_e32 v25, 0x4b400000, v25
	v_add_f32_e32 v32, 0x4b400000, v32
	v_add_u32_e32 v15, 0x90, v14
	v_perm_b32 v17, v24, v17, s33
	v_perm_b32 v24, v32, v25, s33
	v_cvt_f32_i32_e32 v40, v40
	v_perm_b32 v17, v24, v17, s87
	v_mad_i64_i32 v[24:25], s[8:9], v15, s88, v[4:5]
	v_lshl_add_u64 v[24:25], v[24:25], 0, v[2:3]
	global_store_dwordx2 v[24:25], v[16:17], off
	v_fmamk_f32 v17, v45, 0xb80b6d22, v206
	v_exp_f32_e32 v17, v17
	v_fmamk_f32 v24, v43, 0xb80b6d22, v206
	v_exp_f32_e32 v24, v24
	v_fmamk_f32 v25, v40, 0xb80b6d22, v206
	v_exp_f32_e32 v25, v25
	v_fmamk_f32 v32, v38, 0xb80b6d22, v206
	v_exp_f32_e32 v32, v32
	v_fmamk_f32 v33, v36, 0xb80b6d22, v206
	v_add_f32_e32 v17, 0x4ce089af, v17
	v_exp_f32_e32 v33, v33
	v_rcp_f32_e32 v17, v17
	v_add_f32_e32 v24, 0x4ce089af, v24
	v_rcp_f32_e32 v24, v24
	v_add_f32_e32 v25, 0x4ce089af, v25
	v_rcp_f32_e32 v25, v25
	v_add_f32_e32 v32, 0x4ce089af, v32
	v_mul_f32_e32 v16, v46, v45
	v_rcp_f32_e32 v32, v32
	v_add_f32_e32 v33, 0x4ce089af, v33
	v_mul_f32_e32 v16, v17, v16
	v_mul_f32_e32 v17, v44, v43
	v_rcp_f32_e32 v33, v33
	v_mul_f32_e32 v17, v24, v17
	v_mul_f32_e32 v24, v42, v40
	v_mul_f32_e32 v24, v25, v24
	v_mul_f32_e32 v25, v39, v38
	v_mul_f32_e32 v25, v32, v25
	v_mul_f32_e32 v32, v37, v36
	v_mul_f32_e32 v32, v33, v32
;     __device__ __forceinline__ void operator()(const Acc& acc, const Unit& u, int wr, int wc, int fr, int fq) const {
;     ...
;             for (int m = 0; m < 4; ++m) { const size_t off = (size_t)(row0 + ai * HALF + m * 16) * ldc + col0;
;                 float h[8];
; #pragma unroll
;                 for (int n = 0; n < 2; ++n)
; #pragma unroll
;                     for (int e = 0; e < 4; ++e) { const float a0 = acc[ai][0][m][n][e], a1 = acc[ai][1][m][n][e];
;                         h[n * 4 + e] = (a0 * a1) * __builtin_amdgcn_rcpf(c3 + __builtin_amdgcn_exp2f(fmaf(a0, c1, c0))); }
;                 if constexpr (FP8OUT == 2) { u32x2 w; w.x = pk4_i8(h[0], h[1], h[2], h[3]); w.y = pk4_i8(h[4], h[5], h[6], h[7]); *(u32x2*)((unsigned char*)H + off) = w; }
; template <int MODE>
; __device__ __forceinline__ void tr_matrix6(const float* W, int nb, int K, int N, unsigned char* WT, int drows, int rot, int gw, int NGW, int lane, float wscale) {
;     ...
;         const int drow0 = (MODE == 0) ? n0 : ((n0 >> 7) * 256 + (n0 & 127) + (MODE == 2 ? 128 : 0));
;         unsigned char* dst = WT + (size_t)e * drows * K + (size_t)(drow0 + 4 * c) * K + k0 + 32 * q;
; #pragma unroll
;         for (int j = 0; j < 4; ++j) { float x[32];
; #pragma unroll
;             for (int i = 0; i < 32; ++i) x[i] = v[i][j] * wscale;
;             const v6u w = pk32_fp6(x);
;             *(u32x4*)(dst + (size_t)j * K) = (u32x4){w[0], w[1], w[2], w[3]}; *(u32x4*)(dst + (size_t)j * K + 16) = (u32x4){w[4], w[5], 0u, 0u}; }
	v_mul_f32_e32 v33, v35, v34
	v_fmamk_f32 v34, v34, 0xb80b6d22, v206
	v_mul_f32_e32 v31, v31, v30
	v_fmamk_f32 v30, v30, 0xb80b6d22, v206
	v_mul_f32_e32 v29, v29, v28
	v_fmamk_f32 v28, v28, 0xb80b6d22, v206
	v_exp_f32_e32 v34, v34
	v_exp_f32_e32 v30, v30
	v_exp_f32_e32 v28, v28
	v_med3_f32 v16, v16, s1, v207
	v_add_f32_e32 v34, 0x4ce089af, v34
	v_add_f32_e32 v30, 0x4ce089af, v30
	v_add_f32_e32 v28, 0x4ce089af, v28
	v_rcp_f32_e32 v34, v34
	v_rcp_f32_e32 v30, v30
	v_rcp_f32_e32 v28, v28
	v_med3_f32 v17, v17, s1, v207
	v_med3_f32 v24, v24, s1, v207
	v_med3_f32 v25, v25, s1, v207
	v_add_f32_e32 v16, 0x4b400000, v16
	v_add_f32_e32 v17, 0x4b400000, v17
	v_add_f32_e32 v24, 0x4b400000, v24
	v_add_f32_e32 v25, 0x4b400000, v25
	v_mul_f32_e32 v33, v34, v33
	v_mul_f32_e32 v30, v30, v31
	v_mul_f32_e32 v28, v28, v29
	v_perm_b32 v16, v17, v16, s33
	v_perm_b32 v17, v25, v24, s33
	v_perm_b32 v16, v17, v16, s87
	v_med3_f32 v17, v32, s1, v207
	v_med3_f32 v24, v33, s1, v207
	v_med3_f32 v25, v30, s1, v207
	v_med3_f32 v28, v28, s1, v207
	v_add_f32_e32 v17, 0x4b400000, v17
	v_add_f32_e32 v24, 0x4b400000, v24
	v_add_f32_e32 v25, 0x4b400000, v25
	v_add_f32_e32 v28, 0x4b400000, v28
	v_add_u32_e32 v15, 0xa0, v14
	v_perm_b32 v17, v24, v17, s33
	v_perm_b32 v24, v28, v25, s33
	v_perm_b32 v17, v24, v17, s87
	v_mad_i64_i32 v[24:25], s[8:9], v15, s88, v[4:5]
	v_lshl_add_u64 v[24:25], v[24:25], 0, v[2:3]
	global_store_dwordx2 v[24:25], v[16:17], off
	v_fmamk_f32 v16, v26, 0xb80b6d22, v206
	v_exp_f32_e32 v16, v16
	v_fmamk_f32 v17, v22, 0xb80b6d22, v206
	v_exp_f32_e32 v17, v17
	v_mul_f32_e32 v15, v27, v26
	v_add_f32_e32 v16, 0x4ce089af, v16
	v_rcp_f32_e32 v16, v16
	v_add_f32_e32 v17, 0x4ce089af, v17
	v_rcp_f32_e32 v17, v17
	v_mul_f32_e32 v19, v19, v18
	v_mul_f32_e32 v15, v16, v15
	v_mul_f32_e32 v16, v23, v22
	v_mul_f32_e32 v16, v17, v16
	v_mul_f32_e32 v17, v21, v20
	v_fmamk_f32 v20, v20, 0xb80b6d22, v206
	v_fmamk_f32 v18, v18, 0xb80b6d22, v206
	v_exp_f32_e32 v20, v20
	v_exp_f32_e32 v18, v18
	v_mul_f32_e32 v13, v13, v12
	v_fmamk_f32 v12, v12, 0xb80b6d22, v206
	v_mul_f32_e32 v11, v11, v10
	v_fmamk_f32 v10, v10, 0xb80b6d22, v206
	v_mul_f32_e32 v9, v9, v8
	v_fmamk_f32 v8, v8, 0xb80b6d22, v206
	v_mul_f32_e32 v7, v7, v6
	v_fmamk_f32 v6, v6, 0xb80b6d22, v206
	v_exp_f32_e32 v12, v12
	v_exp_f32_e32 v10, v10
	v_exp_f32_e32 v8, v8
	v_exp_f32_e32 v6, v6
	v_add_f32_e32 v20, 0x4ce089af, v20
	v_add_f32_e32 v18, 0x4ce089af, v18
	v_rcp_f32_e32 v20, v20
	v_rcp_f32_e32 v18, v18
	v_add_f32_e32 v12, 0x4ce089af, v12
	v_add_f32_e32 v10, 0x4ce089af, v10
	v_add_f32_e32 v8, 0x4ce089af, v8
	v_add_f32_e32 v6, 0x4ce089af, v6
	v_rcp_f32_e32 v12, v12
	v_rcp_f32_e32 v10, v10
	v_rcp_f32_e32 v8, v8
	v_rcp_f32_e32 v6, v6
	v_mul_f32_e32 v17, v20, v17
	v_mul_f32_e32 v18, v18, v19
	v_mul_f32_e32 v12, v12, v13
	v_mul_f32_e32 v10, v10, v11
	v_mul_f32_e32 v8, v8, v9
	v_mul_f32_e32 v7, v6, v7
	v_med3_f32 v6, v15, s1, v207
	v_med3_f32 v9, v16, s1, v207
	v_med3_f32 v11, v17, s1, v207
	v_med3_f32 v13, v18, s1, v207
	v_add_f32_e32 v6, 0x4b400000, v6
	v_add_f32_e32 v9, 0x4b400000, v9
	v_add_f32_e32 v11, 0x4b400000, v11
	v_add_f32_e32 v13, 0x4b400000, v13
	v_perm_b32 v6, v9, v6, s33
	v_perm_b32 v9, v13, v11, s33
	v_perm_b32 v6, v9, v6, s87
	v_med3_f32 v9, v12, s1, v207
	v_med3_f32 v10, v10, s1, v207
	v_med3_f32 v8, v8, s1, v207
	v_med3_f32 v7, v7, s1, v207
	v_add_u32_e32 v14, 0xb0, v14
	v_add_f32_e32 v9, 0x4b400000, v9
	v_add_f32_e32 v10, 0x4b400000, v10
	v_add_f32_e32 v8, 0x4b400000, v8
	v_add_f32_e32 v7, 0x4b400000, v7
	v_perm_b32 v9, v10, v9, s33
	v_perm_b32 v7, v7, v8, s33
	v_mad_i64_i32 v[4:5], s[8:9], v14, s88, v[4:5]
	v_perm_b32 v7, v7, v9, s87
	v_lshl_add_u64 v[2:3], v[4:5], 0, v[2:3]
	s_cmp_lt_u32 s98, 28
	s_cbranch_scc0 .Lp8f_e
	s_waitcnt vmcnt(3)
	v_mul_f32_e32 v208, 0x42b40000, v208
	v_mul_f32_e32 v209, 0x42b40000, v209
	v_mul_f32_e32 v210, 0x42b40000, v210
	v_mul_f32_e32 v211, 0x42b40000, v211
	v_mul_f32_e32 v212, 0x42b40000, v212
	v_mul_f32_e32 v213, 0x42b40000, v213
	v_mul_f32_e32 v214, 0x42b40000, v214
	v_mul_f32_e32 v215, 0x42b40000, v215
	v_mul_f32_e32 v216, 0x42b40000, v216
	v_mul_f32_e32 v217, 0x42b40000, v217
	v_mul_f32_e32 v218, 0x42b40000, v218
	v_mul_f32_e32 v219, 0x42b40000, v219
	v_mul_f32_e32 v220, 0x42b40000, v220
	v_mul_f32_e32 v221, 0x42b40000, v221
	v_mul_f32_e32 v222, 0x42b40000, v222
	v_mul_f32_e32 v223, 0x42b40000, v223
	v_mul_f32_e32 v224, 0x42b40000, v224
	v_mul_f32_e32 v225, 0x42b40000, v225
	v_mul_f32_e32 v226, 0x42b40000, v226
	v_mul_f32_e32 v227, 0x42b40000, v227
	v_mul_f32_e32 v228, 0x42b40000, v228
	v_mul_f32_e32 v229, 0x42b40000, v229
	v_mul_f32_e32 v230, 0x42b40000, v230
	v_mul_f32_e32 v231, 0x42b40000, v231
	v_mul_f32_e32 v232, 0x42b40000, v232
	v_mul_f32_e32 v233, 0x42b40000, v233
	v_mul_f32_e32 v234, 0x42b40000, v234
	v_mul_f32_e32 v235, 0x42b40000, v235
	v_mul_f32_e32 v236, 0x42b40000, v236
	v_mul_f32_e32 v237, 0x42b40000, v237
	v_mul_f32_e32 v238, 0x42b40000, v238
	v_mul_f32_e32 v239, 0x42b40000, v239
	v_med3_f32 v208, v208, v255, v254
	v_med3_f32 v209, v209, v255, v254
	v_med3_f32 v210, v210, v255, v254
	v_med3_f32 v211, v211, v255, v254
	v_med3_f32 v212, v212, v255, v254
	v_med3_f32 v213, v213, v255, v254
	v_med3_f32 v214, v214, v255, v254
	v_med3_f32 v215, v215, v255, v254
	v_med3_f32 v216, v216, v255, v254
	v_med3_f32 v217, v217, v255, v254
	v_med3_f32 v218, v218, v255, v254
	v_med3_f32 v219, v219, v255, v254
	v_med3_f32 v220, v220, v255, v254
	v_med3_f32 v221, v221, v255, v254
	v_med3_f32 v222, v222, v255, v254
	v_med3_f32 v223, v223, v255, v254
	v_med3_f32 v224, v224, v255, v254
	v_med3_f32 v225, v225, v255, v254
	v_med3_f32 v226, v226, v255, v254
	v_med3_f32 v227, v227, v255, v254
	v_med3_f32 v228, v228, v255, v254
	v_med3_f32 v229, v229, v255, v254
	v_med3_f32 v230, v230, v255, v254
	v_med3_f32 v231, v231, v255, v254
	v_med3_f32 v232, v232, v255, v254
	v_med3_f32 v233, v233, v255, v254
	v_med3_f32 v234, v234, v255, v254
	v_med3_f32 v235, v235, v255, v254
	v_med3_f32 v236, v236, v255, v254
	v_med3_f32 v237, v237, v255, v254
	v_med3_f32 v238, v238, v255, v254
	v_med3_f32 v239, v239, v255, v254
	v_cvt_scalef32_2xpk16_fp6_f32 v[240:245], v[208:223], v[224:239], 1.0
	v_readlane_b32 s100, v252, 6
	v_readlane_b32 s101, v252, 7
	s_lshr_b32 s99, s98, 1
	s_lshl_b32 s99, s99, 19
	s_add_u32 s100, s100, s99
	s_addc_u32 s101, s101, 0
	s_and_b32 s99, s98, 1
	s_lshl_b32 s99, s99, 17
	s_add_u32 s100, s100, s99
	s_addc_u32 s101, s101, 0
	global_store_dwordx4 v249, v[240:243], s[100:101]
	global_store_dwordx4 v249, v[244:247], s[100:101] offset:16
	s_add_i32 s98, s98, 1
.Lp8f_e:
	s_mov_b64 s[56:57], -1
	s_andn2_b64 vcc, exec, s[4:5]
	global_store_dwordx2 v[2:3], v[6:7], off
	s_cbranch_vccnz .LBB0_590
	s_andn2_b64 vcc, exec, s[6:7]
	s_cbranch_vccnz .LBB0_589
	s_barrier
	s_branch .LBB0_589

; template <int MODE>
; __device__ __forceinline__ void tr_matrix6(const float* W, int nb, int K, int N, unsigned char* WT, int drows, int rot, int gw, int NGW, int lane, float wscale) {
;     const int nbn = N / 32, per = (K / 256) * nbn, total = nb * per;
;     int it = gw - rot; if (it < 0) it += NGW;
;     const int c = lane & 7, q = lane >> 3;
;     for (; it < total; it += NGW) {
;         const int e = it / per, r = it - e * per, kb = r / nbn, nbk = r - kb * nbn, n0 = nbk * 32, k0 = kb * 256;
;         const float* src = W + (size_t)e * K * N + (size_t)(k0 + 32 * q) * N + n0 + 4 * c;
;         f32x4 v[32];
; #pragma unroll
;         for (int i = 0; i < 32; ++i) v[i] = *(const f32x4*)(src + (size_t)i * N);
;         const int drow0 = (MODE == 0) ? n0 : ((n0 >> 7) * 256 + (n0 & 127) + (MODE == 2 ? 128 : 0));
;         unsigned char* dst = WT + (size_t)e * drows * K + (size_t)(drow0 + 4 * c) * K + k0 + 32 * q;
; #pragma unroll
;         for (int j = 0; j < 4; ++j) { float x[32];
; #pragma unroll
;             for (int i = 0; i < 32; ++i) x[i] = v[i][j] * wscale;
;             const v6u w = pk32_fp6(x);
;             *(u32x4*)(dst + (size_t)j * K) = (u32x4){w[0], w[1], w[2], w[3]}; *(u32x4*)(dst + (size_t)j * K + 16) = (u32x4){w[4], w[5], 0u, 0u}; }
.LBB0_601:
.Lp8f_fb:
	s_cmp_lt_u32 s98, 28
	s_cbranch_scc0 .Lp8f_fbd
	v_readlane_b32 s100, v252, 4
	v_readlane_b32 s101, v252, 5
	s_lshl_b32 s99, s98, 8
	s_nop 1
	s_add_u32 s100, s100, s99
	s_addc_u32 s101, s101, 0
	global_load_dword v208, v248, s[100:101]
	s_add_u32 s100, s100, 0x7000
	s_addc_u32 s101, s101, 0
	global_load_dword v209, v248, s[100:101]
	s_add_u32 s100, s100, 0x7000
	s_addc_u32 s101, s101, 0
	global_load_dword v210, v248, s[100:101]
	s_add_u32 s100, s100, 0x7000
	s_addc_u32 s101, s101, 0
	global_load_dword v211, v248, s[100:101]
	s_add_u32 s100, s100, 0x7000
	s_addc_u32 s101, s101, 0
	global_load_dword v212, v248, s[100:101]
	s_add_u32 s100, s100, 0x7000
	s_addc_u32 s101, s101, 0
	global_load_dword v213, v248, s[100:101]
	s_add_u32 s100, s100, 0x7000
	s_addc_u32 s101, s101, 0
	global_load_dword v214, v248, s[100:101]
	s_add_u32 s100, s100, 0x7000
	s_addc_u32 s101, s101, 0
	global_load_dword v215, v248, s[100:101]
	s_add_u32 s100, s100, 0x7000
	s_addc_u32 s101, s101, 0
	global_load_dword v216, v248, s[100:101]
	s_add_u32 s100, s100, 0x7000
	s_addc_u32 s101, s101, 0
	global_load_dword v217, v248, s[100:101]
	s_add_u32 s100, s100, 0x7000
	s_addc_u32 s101, s101, 0
	global_load_dword v218, v248, s[100:101]
	s_add_u32 s100, s100, 0x7000
	s_addc_u32 s101, s101, 0
	global_load_dword v219, v248, s[100:101]
	s_add_u32 s100, s100, 0x7000
	s_addc_u32 s101, s101, 0
	global_load_dword v220, v248, s[100:101]
	s_add_u32 s100, s100, 0x7000
	s_addc_u32 s101, s101, 0
	global_load_dword v221, v248, s[100:101]
	s_add_u32 s100, s100, 0x7000
	s_addc_u32 s101, s101, 0
	global_load_dword v222, v248, s[100:101]
	s_add_u32 s100, s100, 0x7000
	s_addc_u32 s101, s101, 0
	global_load_dword v223, v248, s[100:101]
	s_add_u32 s100, s100, 0x7000
	s_addc_u32 s101, s101, 0
	global_load_dword v224, v248, s[100:101]
	s_add_u32 s100, s100, 0x7000
	s_addc_u32 s101, s101, 0
	global_load_dword v225, v248, s[100:101]
	s_add_u32 s100, s100, 0x7000
	s_addc_u32 s101, s101, 0
	global_load_dword v226, v248, s[100:101]
	s_add_u32 s100, s100, 0x7000
	s_addc_u32 s101, s101, 0
	global_load_dword v227, v248, s[100:101]
	s_add_u32 s100, s100, 0x7000
	s_addc_u32 s101, s101, 0
	global_load_dword v228, v248, s[100:101]
	s_add_u32 s100, s100, 0x7000
	s_addc_u32 s101, s101, 0
	global_load_dword v229, v248, s[100:101]
	s_add_u32 s100, s100, 0x7000
	s_addc_u32 s101, s101, 0
	global_load_dword v230, v248, s[100:101]
	s_add_u32 s100, s100, 0x7000
	s_addc_u32 s101, s101, 0
	global_load_dword v231, v248, s[100:101]
	s_add_u32 s100, s100, 0x7000
	s_addc_u32 s101, s101, 0
	global_load_dword v232, v248, s[100:101]
	s_add_u32 s100, s100, 0x7000
	s_addc_u32 s101, s101, 0
	global_load_dword v233, v248, s[100:101]
	s_add_u32 s100, s100, 0x7000
	s_addc_u32 s101, s101, 0
	global_load_dword v234, v248, s[100:101]
	s_add_u32 s100, s100, 0x7000
	s_addc_u32 s101, s101, 0
	global_load_dword v235, v248, s[100:101]
	s_add_u32 s100, s100, 0x7000
	s_addc_u32 s101, s101, 0
	global_load_dword v236, v248, s[100:101]
	s_add_u32 s100, s100, 0x7000
	s_addc_u32 s101, s101, 0
	global_load_dword v237, v248, s[100:101]
	s_add_u32 s100, s100, 0x7000
	s_addc_u32 s101, s101, 0
	global_load_dword v238, v248, s[100:101]
	s_add_u32 s100, s100, 0x7000
	s_addc_u32 s101, s101, 0
	global_load_dword v239, v248, s[100:101]
	s_waitcnt vmcnt(0)
	v_mul_f32_e32 v208, 0x42b40000, v208
	v_mul_f32_e32 v209, 0x42b40000, v209
	v_mul_f32_e32 v210, 0x42b40000, v210
	v_mul_f32_e32 v211, 0x42b40000, v211
	v_mul_f32_e32 v212, 0x42b40000, v212
	v_mul_f32_e32 v213, 0x42b40000, v213
	v_mul_f32_e32 v214, 0x42b40000, v214
	v_mul_f32_e32 v215, 0x42b40000, v215
	v_mul_f32_e32 v216, 0x42b40000, v216
	v_mul_f32_e32 v217, 0x42b40000, v217
	v_mul_f32_e32 v218, 0x42b40000, v218
	v_mul_f32_e32 v219, 0x42b40000, v219
	v_mul_f32_e32 v220, 0x42b40000, v220
	v_mul_f32_e32 v221, 0x42b40000, v221
	v_mul_f32_e32 v222, 0x42b40000, v222
	v_mul_f32_e32 v223, 0x42b40000, v223
	v_mul_f32_e32 v224, 0x42b40000, v224
	v_mul_f32_e32 v225, 0x42b40000, v225
	v_mul_f32_e32 v226, 0x42b40000, v226
	v_mul_f32_e32 v227, 0x42b40000, v227
	v_mul_f32_e32 v228, 0x42b40000, v228
	v_mul_f32_e32 v229, 0x42b40000, v229
	v_mul_f32_e32 v230, 0x42b40000, v230
	v_mul_f32_e32 v231, 0x42b40000, v231
	v_mul_f32_e32 v232, 0x42b40000, v232
	v_mul_f32_e32 v233, 0x42b40000, v233
	v_mul_f32_e32 v234, 0x42b40000, v234
	v_mul_f32_e32 v235, 0x42b40000, v235
	v_mul_f32_e32 v236, 0x42b40000, v236
	v_mul_f32_e32 v237, 0x42b40000, v237
	v_mul_f32_e32 v238, 0x42b40000, v238
	v_mul_f32_e32 v239, 0x42b40000, v239
	v_med3_f32 v208, v208, v255, v254
	v_med3_f32 v209, v209, v255, v254
	v_med3_f32 v210, v210, v255, v254
	v_med3_f32 v211, v211, v255, v254
	v_med3_f32 v212, v212, v255, v254
	v_med3_f32 v213, v213, v255, v254
	v_med3_f32 v214, v214, v255, v254
	v_med3_f32 v215, v215, v255, v254
	v_med3_f32 v216, v216, v255, v254
	v_med3_f32 v217, v217, v255, v254
	v_med3_f32 v218, v218, v255, v254
	v_med3_f32 v219, v219, v255, v254
	v_med3_f32 v220, v220, v255, v254
	v_med3_f32 v221, v221, v255, v254
	v_med3_f32 v222, v222, v255, v254
	v_med3_f32 v223, v223, v255, v254
	v_med3_f32 v224, v224, v255, v254
	v_med3_f32 v225, v225, v255, v254
	v_med3_f32 v226, v226, v255, v254
	v_med3_f32 v227, v227, v255, v254
	v_med3_f32 v228, v228, v255, v254
	v_med3_f32 v229, v229, v255, v254
	v_med3_f32 v230, v230, v255, v254
	v_med3_f32 v231, v231, v255, v254
	v_med3_f32 v232, v232, v255, v254
	v_med3_f32 v233, v233, v255, v254
	v_med3_f32 v234, v234, v255, v254
	v_med3_f32 v235, v235, v255, v254
	v_med3_f32 v236, v236, v255, v254
	v_med3_f32 v237, v237, v255, v254
	v_med3_f32 v238, v238, v255, v254
	v_med3_f32 v239, v239, v255, v254
	v_cvt_scalef32_2xpk16_fp6_f32 v[240:245], v[208:223], v[224:239], 1.0
	v_readlane_b32 s100, v252, 6
	v_readlane_b32 s101, v252, 7
	s_lshr_b32 s99, s98, 1
	s_lshl_b32 s99, s99, 19
	s_add_u32 s100, s100, s99
	s_addc_u32 s101, s101, 0
	s_and_b32 s99, s98, 1
	s_lshl_b32 s99, s99, 17
	s_add_u32 s100, s100, s99
	s_addc_u32 s101, s101, 0
	global_store_dwordx4 v249, v[240:243], s[100:101]
	global_store_dwordx4 v249, v[244:247], s[100:101] offset:16
	s_add_i32 s98, s98, 1
	s_branch .Lp8f_fb
